# code placement: the hand-written loop heads (PEER u/v loops, attention steps, threshold search) aligned to 8 bytes (.p2align 3); the v loop and attention steps sat at 4 mod 8
# baseline (speedup 1.0000x reference)
.Ltk_mk_done:
	s_mov_b32 s11, 0
	s_brev_b32 s4, 1
	.p2align 3

.Lcv_a_nop:
	s_waitcnt lgkmcnt(0)
	v_add_u32_e32 v2, 31, v172
	v_and_b32_e32 v173, 15, v151
	v_ashrrev_i32_e32 v174, 4, v151
	v_ashrrev_i32_e32 v176, 5, v2
	v_mov_b32_e32 v29, 0
	v_lshlrev_b32_e32 v148, 7, v173
	v_mov_b32_e32 v149, v147
	v_cmp_lt_i32_e32 vcc, 0, v176
	v_lshlrev_b32_e32 v150, 2, v174
	v_mov_b32_e32 v28, v29
	v_mov_b32_e32 v27, v29
	v_mov_b32_e32 v26, v29
	v_mov_b32_e32 v33, v29
	v_mov_b32_e32 v32, v29
	v_mov_b32_e32 v31, v29
	v_mov_b32_e32 v30, v29
	v_mov_b32_e32 v25, v29
	v_mov_b32_e32 v24, v29
	v_mov_b32_e32 v23, v29
	v_mov_b32_e32 v22, v29
	v_mov_b32_e32 v21, v29
	v_mov_b32_e32 v20, v29
	v_mov_b32_e32 v19, v29
	v_mov_b32_e32 v18, v29
	v_mov_b32_e32 v17, v29
	v_mov_b32_e32 v16, v29
	v_mov_b32_e32 v15, v29
	v_mov_b32_e32 v14, v29
	v_mov_b32_e32 v13, v29
	v_mov_b32_e32 v12, v29
	v_mov_b32_e32 v11, v29
	v_mov_b32_e32 v10, v29
	v_mov_b32_e32 v9, v29
	v_mov_b32_e32 v8, v29
	v_mov_b32_e32 v7, v29
	v_mov_b32_e32 v6, v29
	v_mov_b32_e32 v5, v29
	v_mov_b32_e32 v4, v29
	v_mov_b32_e32 v3, v29
	v_mov_b32_e32 v2, v29
	v_mov_b32_e32 v179, v29
	s_and_saveexec_b64 s[0:1], vcc
	s_cbranch_execz .LBB0_1127
	v_readfirstlane_b32 s10, v176
	v_readfirstlane_b32 s36, v172
	v_readlane_b32 s37, v242, 49
	s_mul_i32 s5, s78, 0x3400000
	s_mul_hi_i32 s4, s78, 0x3400000
	s_add_u32 s2, s82, s5
	s_addc_u32 s3, s83, s4
	s_add_u32 s4, s2, 0x2800
	s_addc_u32 s5, s3, 0
	s_add_u32 s6, s2, 0x2900
	s_addc_u32 s7, s3, 0
	s_mul_i32 s20, s97, 0x3400
	s_mul_hi_u32 s21, s96, 0x3400
	s_add_i32 s21, s21, s20
	s_mul_i32 s20, s96, 0x3400
	s_add_u32 s20, s82, s20
	s_addc_u32 s21, s83, s21
	s_add_u32 s20, s20, 0x1800
	s_addc_u32 s21, s21, 0
	s_add_u32 s26, s89, 0x400
	s_lshl_b32 s27, s37, 13
	s_add_u32 s27, s27, 0x14000
	v_lshlrev_b32_e32 v96, 2, v150
	v_lshl_add_u32 v153, v148, 1, v96
	global_load_dwordx4 v[42:45], v153, s[20:21]
	global_load_dwordx4 v[34:37], v153, s[20:21] offset:64
	global_load_dwordx4 v[38:41], v153, s[20:21] offset:128
	global_load_dwordx4 v[46:49], v153, s[20:21] offset:192
	v_add_u32_e32 v239, s89, v150
	ds_read2_b32 v[98:99], v239 offset0:0 offset1:4
	ds_read2_b32 v[100:101], v239 offset0:8 offset1:12
	ds_read2_b32 v[102:103], v239 offset0:16 offset1:20
	ds_read2_b32 v[104:105], v239 offset0:24 offset1:28
	ds_read2_b32 v[106:107], v239 offset0:32 offset1:36
	ds_read2_b32 v[108:109], v239 offset0:40 offset1:44
	ds_read2_b32 v[110:111], v239 offset0:48 offset1:52
	ds_read2_b32 v[112:113], v239 offset0:56 offset1:60
	v_mov_b32_e32 v96, v174
	v_xor_b32_e32 v96, v96, v173
	v_lshlrev_b32_e32 v220, 4, v96
	v_add_u32_e32 v96, 4, v174
	v_xor_b32_e32 v96, v96, v173
	v_lshlrev_b32_e32 v221, 4, v96
	v_add_u32_e32 v96, 8, v174
	v_xor_b32_e32 v96, v96, v173
	v_lshlrev_b32_e32 v222, 4, v96
	v_add_u32_e32 v96, 12, v174
	v_xor_b32_e32 v96, v96, v173
	v_lshlrev_b32_e32 v223, 4, v96
	v_lshlrev_b32_e32 v224, 4, v173
	v_lshlrev_b32_e32 v96, 1, v174
	v_xor_b32_e32 v96, v96, v173
	v_lshlrev_b32_e32 v96, 4, v96
	v_lshl_add_u32 v97, v174, 8, s27
	v_add_u32_e32 v225, v97, v96
	v_xor_b32_e32 v96, 0x80, v96
	v_add_u32_e32 v226, v97, v96
	v_lshl_add_u32 v97, v173, 8, s26
	v_mov_b32_e32 v96, v174
	v_xor_b32_e32 v96, v96, v173
	v_lshl_add_u32 v227, v96, 4, v97
	v_add_u32_e32 v96, 4, v174
	v_xor_b32_e32 v96, v96, v173
	v_lshl_add_u32 v228, v96, 4, v97
	v_add_u32_e32 v96, 8, v174
	v_xor_b32_e32 v96, v96, v173
	v_lshl_add_u32 v229, v96, 4, v97
	v_add_u32_e32 v96, 12, v174
	v_xor_b32_e32 v96, v96, v173
	v_lshl_add_u32 v230, v96, 4, v97
	v_lshrrev_b32_e32 v241, 2, v173
	v_add_u32_e32 v241, v241, v150
	v_and_b32_e32 v177, 7, v241
	v_and_b32_e32 v96, 3, v173
	v_lshlrev_b32_e32 v96, 3, v96
	v_lshl_add_u32 v241, v241, 8, v96
	v_add_u32_e32 v241, s27, v241
	v_xor_b32_e32 v96, 0, v177
	v_lshl_add_u32 v231, v96, 5, v241
	v_xor_b32_e32 v96, 1, v177
	v_lshl_add_u32 v232, v96, 5, v241
	v_xor_b32_e32 v96, 2, v177
	v_lshl_add_u32 v233, v96, 5, v241
	v_xor_b32_e32 v96, 3, v177
	v_lshl_add_u32 v234, v96, 5, v241
	v_xor_b32_e32 v96, 4, v177
	v_lshl_add_u32 v235, v96, 5, v241
	v_xor_b32_e32 v96, 5, v177
	v_lshl_add_u32 v236, v96, 5, v241
	v_xor_b32_e32 v96, 6, v177
	v_lshl_add_u32 v237, v96, 5, v241
	v_xor_b32_e32 v96, 7, v177
	v_lshl_add_u32 v238, v96, 5, v241
	v_mov_b32_e32 v2, 0
	v_mov_b32_e32 v3, 0
	v_mov_b32_e32 v4, 0
	v_mov_b32_e32 v5, 0
	v_mov_b32_e32 v6, 0
	v_mov_b32_e32 v7, 0
	v_mov_b32_e32 v8, 0
	v_mov_b32_e32 v9, 0
	v_mov_b32_e32 v10, 0
	v_mov_b32_e32 v11, 0
	v_mov_b32_e32 v12, 0
	v_mov_b32_e32 v13, 0
	v_mov_b32_e32 v14, 0
	v_mov_b32_e32 v15, 0
	v_mov_b32_e32 v16, 0
	v_mov_b32_e32 v17, 0
	v_mov_b32_e32 v18, 0
	v_mov_b32_e32 v19, 0
	v_mov_b32_e32 v20, 0
	v_mov_b32_e32 v21, 0
	v_mov_b32_e32 v22, 0
	v_mov_b32_e32 v23, 0
	v_mov_b32_e32 v24, 0
	v_mov_b32_e32 v25, 0
	v_mov_b32_e32 v26, 0
	v_mov_b32_e32 v27, 0
	v_mov_b32_e32 v28, 0
	v_mov_b32_e32 v29, 0
	v_mov_b32_e32 v30, 0
	v_mov_b32_e32 v31, 0
	v_mov_b32_e32 v32, 0
	v_mov_b32_e32 v33, 0
	v_mov_b32_e32 v179, 0
	v_mov_b32_e32 v181, 0xf149f2ca
	v_mov_b32_e32 v95, 0
	s_mov_b32 s11, 0
	s_mov_b32 s22, 0
	s_waitcnt lgkmcnt(0)
	s_mov_b32 m0, s26
	v_mad_u32_u24 v240, v98, s35, v220
	global_load_lds_dwordx4 v240, s[4:5]
	s_add_u32 m0, s26, 1024
	v_mad_u32_u24 v240, v99, s35, v221
	global_load_lds_dwordx4 v240, s[4:5]
	s_add_u32 m0, s26, 2048
	v_mad_u32_u24 v240, v100, s35, v222
	global_load_lds_dwordx4 v240, s[4:5]
	s_add_u32 m0, s26, 3072
	v_mad_u32_u24 v240, v101, s35, v223
	global_load_lds_dwordx4 v240, s[4:5]
	s_add_u32 m0, s26, 4096
	v_mad_u32_u24 v240, v102, s35, v220
	global_load_lds_dwordx4 v240, s[4:5]
	s_add_u32 m0, s26, 5120
	v_mad_u32_u24 v240, v103, s35, v221
	global_load_lds_dwordx4 v240, s[4:5]
	s_add_u32 m0, s26, 6144
	v_mad_u32_u24 v240, v104, s35, v222
	global_load_lds_dwordx4 v240, s[4:5]
	s_add_u32 m0, s26, 7168
	v_mad_u32_u24 v240, v105, s35, v223
	global_load_lds_dwordx4 v240, s[4:5]
	v_mad_u32_u24 v240, v98, s35, v224
	global_load_dwordx4 v[114:117], v240, s[6:7]
	v_mad_u32_u24 v240, v99, s35, v224
	global_load_dwordx4 v[118:121], v240, s[6:7]
	v_mad_u32_u24 v240, v100, s35, v224
	global_load_dwordx4 v[122:125], v240, s[6:7]
	v_mad_u32_u24 v240, v101, s35, v224
	global_load_dwordx4 v[126:129], v240, s[6:7]
	v_mad_u32_u24 v240, v102, s35, v224
	global_load_dwordx4 v[130:133], v240, s[6:7]
	v_mad_u32_u24 v240, v103, s35, v224
	global_load_dwordx4 v[134:137], v240, s[6:7]
	v_mad_u32_u24 v240, v104, s35, v224
	global_load_dwordx4 v[138:141], v240, s[6:7]
	v_mad_u32_u24 v240, v105, s35, v224
	global_load_dwordx4 v[142:145], v240, s[6:7]
	s_cmp_ge_u32 s10, 2
	s_cbranch_scc0 .Lat_A
	v_mad_u32_u24 v240, v106, s35, v224
	global_load_dwordx4 v[188:191], v240, s[6:7]
	v_mad_u32_u24 v240, v107, s35, v224
	global_load_dwordx4 v[192:195], v240, s[6:7]
	v_mad_u32_u24 v240, v108, s35, v224
	global_load_dwordx4 v[196:199], v240, s[6:7]
	v_mad_u32_u24 v240, v109, s35, v224
	global_load_dwordx4 v[200:203], v240, s[6:7]
	v_mad_u32_u24 v240, v110, s35, v224
	global_load_dwordx4 v[204:207], v240, s[6:7]
	v_mad_u32_u24 v240, v111, s35, v224
	global_load_dwordx4 v[208:211], v240, s[6:7]
	v_mad_u32_u24 v240, v112, s35, v224
	global_load_dwordx4 v[212:215], v240, s[6:7]
	v_mad_u32_u24 v240, v113, s35, v224
	global_load_dwordx4 v[216:219], v240, s[6:7]
	.p2align 3

.Lat_A_full:
	v_max3_f32 v92, v82, v83, v84
	v_max3_f32 v93, v85, v86, v87
	v_max3_f32 v92, v92, v88, v89
	v_max_f32_e32 v92, v92, v93
	v_mov_b32_e32 v93, v92
	s_nop 1
	v_permlane16_swap_b32_e32 v92, v93
	v_max_f32_e32 v92, v92, v93
	v_mov_b32_e32 v93, v92
	s_nop 1
	v_permlane32_swap_b32_e32 v92, v93
	v_max3_f32 v180, v181, v92, v93
	v_sub_f32_e32 v94, v181, v180
	v_sub_f32_e32 v82, v82, v180
	v_sub_f32_e32 v83, v83, v180
	v_sub_f32_e32 v84, v84, v180
	v_sub_f32_e32 v85, v85, v180
	v_sub_f32_e32 v86, v86, v180
	v_sub_f32_e32 v87, v87, v180
	v_sub_f32_e32 v88, v88, v180
	v_sub_f32_e32 v89, v89, v180
	v_exp_f32_e32 v94, v94
	v_exp_f32_e32 v82, v82
	v_exp_f32_e32 v83, v83
	v_exp_f32_e32 v84, v84
	v_exp_f32_e32 v85, v85
	v_exp_f32_e32 v86, v86
	v_exp_f32_e32 v87, v87
	v_exp_f32_e32 v88, v88
	v_exp_f32_e32 v89, v89
	v_add_f32_e32 v92, v82, v83
	v_add_f32_e32 v93, v84, v85
	v_add_f32_e32 v97, v86, v87
	v_add_f32_e32 v92, v92, v93
	v_add_f32_e32 v96, v88, v89
	v_add_f32_e32 v97, v97, v96
	v_add_f32_e32 v92, v92, v97
	v_mov_b32_e32 v93, v92
	v_mov_b32_e32 v181, v180
	v_cvt_pk_bf16_f32 v82, v82, v83
	v_cvt_pk_bf16_f32 v83, v84, v85
	v_permlane16_swap_b32_e32 v92, v93
	v_add_f32_e32 v92, v92, v93
	v_mov_b32_e32 v93, v92
	v_cvt_pk_bf16_f32 v84, v86, v87
	v_cvt_pk_bf16_f32 v85, v88, v89
	v_permlane32_swap_b32_e32 v92, v93
	v_add_f32_e32 v92, v92, v93
	v_fma_f32 v179, v179, v94, v92
	v_pk_mul_f32 v[2:3], v[2:3], v[94:95] op_sel_hi:[1,0]
	v_pk_mul_f32 v[4:5], v[4:5], v[94:95] op_sel_hi:[1,0]
	v_pk_mul_f32 v[6:7], v[6:7], v[94:95] op_sel_hi:[1,0]
	v_pk_mul_f32 v[8:9], v[8:9], v[94:95] op_sel_hi:[1,0]
	v_pk_mul_f32 v[10:11], v[10:11], v[94:95] op_sel_hi:[1,0]
	v_pk_mul_f32 v[12:13], v[12:13], v[94:95] op_sel_hi:[1,0]
	v_pk_mul_f32 v[14:15], v[14:15], v[94:95] op_sel_hi:[1,0]
	v_pk_mul_f32 v[16:17], v[16:17], v[94:95] op_sel_hi:[1,0]
	v_pk_mul_f32 v[18:19], v[18:19], v[94:95] op_sel_hi:[1,0]
	v_pk_mul_f32 v[20:21], v[20:21], v[94:95] op_sel_hi:[1,0]
	v_pk_mul_f32 v[22:23], v[22:23], v[94:95] op_sel_hi:[1,0]
	v_pk_mul_f32 v[24:25], v[24:25], v[94:95] op_sel_hi:[1,0]
	v_pk_mul_f32 v[26:27], v[26:27], v[94:95] op_sel_hi:[1,0]
	v_pk_mul_f32 v[28:29], v[28:29], v[94:95] op_sel_hi:[1,0]
	v_pk_mul_f32 v[30:31], v[30:31], v[94:95] op_sel_hi:[1,0]
	v_pk_mul_f32 v[32:33], v[32:33], v[94:95] op_sel_hi:[1,0]
	ds_read_b64_tr_b16 v[86:87], v231
	ds_read_b64_tr_b16 v[88:89], v231 offset:4096
	ds_read_b64_tr_b16 v[244:245], v232
	ds_read_b64_tr_b16 v[246:247], v232 offset:4096
	s_waitcnt lgkmcnt(2)
	v_mfma_f32_16x16x32_bf16 v[2:5], v[86:89], v[82:85], v[2:5]
	ds_read_b64_tr_b16 v[86:87], v233
	ds_read_b64_tr_b16 v[88:89], v233 offset:4096
	s_waitcnt lgkmcnt(2)
	v_mfma_f32_16x16x32_bf16 v[6:9], v[244:247], v[82:85], v[6:9]
	ds_read_b64_tr_b16 v[244:245], v234
	ds_read_b64_tr_b16 v[246:247], v234 offset:4096
	s_waitcnt lgkmcnt(2)
	v_mfma_f32_16x16x32_bf16 v[10:13], v[86:89], v[82:85], v[10:13]
	ds_read_b64_tr_b16 v[86:87], v235
	ds_read_b64_tr_b16 v[88:89], v235 offset:4096
	s_waitcnt lgkmcnt(2)
	v_mfma_f32_16x16x32_bf16 v[14:17], v[244:247], v[82:85], v[14:17]
	ds_read_b64_tr_b16 v[244:245], v236
	ds_read_b64_tr_b16 v[246:247], v236 offset:4096
	s_waitcnt lgkmcnt(2)
	v_mfma_f32_16x16x32_bf16 v[18:21], v[86:89], v[82:85], v[18:21]
	ds_read_b64_tr_b16 v[86:87], v237
	ds_read_b64_tr_b16 v[88:89], v237 offset:4096
	s_waitcnt lgkmcnt(2)
	v_mfma_f32_16x16x32_bf16 v[22:25], v[244:247], v[82:85], v[22:25]
	ds_read_b64_tr_b16 v[244:245], v238
	ds_read_b64_tr_b16 v[246:247], v238 offset:4096
	s_waitcnt lgkmcnt(2)
	v_mfma_f32_16x16x32_bf16 v[30:33], v[86:89], v[82:85], v[30:33]
	s_waitcnt lgkmcnt(0)
	v_mfma_f32_16x16x32_bf16 v[26:29], v[244:247], v[82:85], v[26:29]
	s_add_u32 s11, s11, 1
	s_add_u32 s22, s22, 32
	v_add_u32_e32 v239, 0x80, v239
	s_cmp_lt_u32 s11, s10
	s_cbranch_scc0 .Lat_done
	.p2align 3

.LBB0_1535:
	v_lshl_or_b32 v7, v7, 11, v50
	v_lshrrev_b32_e32 v8, 15, v7
	v_and_b32_e32 v8, 0x1fffc, v8
	s_add_i32 s0, 0, 0x20500
	v_add_u32_e32 v8, s0, v8
	s_waitcnt lgkmcnt(0)
	s_barrier
	ds_read_b32 v8, v8
	v_add_u32_e32 v58, 0x200, v50
	v_lshlrev_b32_e32 v5, 2, v5
	v_lshl_or_b32 v6, v6, 11, v58
	v_add_u32_e32 v57, 0x400, v50
	s_waitcnt lgkmcnt(0)
	v_lshlrev_b32_e32 v8, 2, v8
	v_add3_u32 v5, s35, v8, v5
	ds_write_b32 v5, v7
	v_lshrrev_b32_e32 v5, 15, v6
	v_and_b32_e32 v5, 0x1fffc, v5
	v_add_u32_e32 v5, s0, v5
	ds_read_b32 v5, v5
	v_lshlrev_b32_e32 v3, 2, v3
	v_lshl_or_b32 v4, v4, 11, v57
	v_add_u32_e32 v55, 0x600, v50
	v_lshlrev_b32_e32 v1, 2, v1
	s_waitcnt lgkmcnt(0)
	v_lshlrev_b32_e32 v5, 2, v5
	v_add3_u32 v3, s35, v5, v3
	ds_write_b32 v3, v6
	v_lshrrev_b32_e32 v3, 15, v4
	v_and_b32_e32 v3, 0x1fffc, v3
	v_add_u32_e32 v3, s0, v3
	ds_read_b32 v3, v3
	v_lshl_or_b32 v2, v2, 11, v55
	v_lshlrev_b32_e32 v0, 2, v0
	v_and_b32_e32 v61, -16, v145
	v_add_u32_e32 v32, s20, v61
	s_waitcnt lgkmcnt(0)
	v_lshlrev_b32_e32 v3, 2, v3
	v_add3_u32 v1, s35, v3, v1
	ds_write_b32 v1, v4
	v_lshrrev_b32_e32 v1, 15, v2
	v_and_b32_e32 v1, 0x1fffc, v1
	v_add_u32_e32 v1, s0, v1
	ds_read_b32 v1, v1
	v_and_b32_e32 v3, 15, v145
	v_lshlrev_b32_e32 v34, 2, v3
	v_readlane_b32 s0, v242, 31
	v_readlane_b32 s1, v242, 32
	s_waitcnt lgkmcnt(0)
	v_lshlrev_b32_e32 v1, 2, v1
	v_add3_u32 v0, s35, v1, v0
	ds_write_b32 v0, v2
	v_add_u32_e32 v2, s35, v34
	s_waitcnt lgkmcnt(0)
	s_barrier
	v_and_b32_e32 v161, 15, v145
	v_and_b32_e32 v162, -16, v145
	v_mov_b32_e32 v157, 0
	v_lshl_add_u32 v155, v161, 2, s35
	v_add_u32_e32 v156, s20, v162
	v_add_u32_e32 v154, s21, v162
	v_lshl_add_u64 v[152:153], s[0:1], 0, v[156:157]
	v_lshrrev_b32_e32 v170, 2, v145
	v_lshl_add_u32 v170, v170, 2, s35
	v_and_b32_e32 v174, 3, v145
	v_lshl_add_u32 v174, v174, 4, s20
	v_mov_b32_e32 v175, 0
	v_lshl_add_u64 v[172:173], s[0:1], 0, v[174:175]
	v_lshrrev_b32_e32 v171, 4, v145
	v_lshl_add_u32 v171, v161, 2, v171
	v_lshlrev_b32_e32 v171, 2, v171
	ds_read_b32 v182, v155
	ds_read_b32 v166, v170
	ds_read_b32 v183, v155 offset:64
	ds_read_b32 v167, v170 offset:64
	ds_read_b32 v184, v155 offset:128
	ds_read_b32 v168, v170 offset:128
	v_and_b32_e32 v163, 1, v145
	v_cmp_ne_u32_e64 s[2:3], 0, v163
	v_and_b32_e32 v163, 2, v145
	v_cmp_ne_u32_e64 s[10:11], 0, v163
	v_lshrrev_b32_e32 v163, 4, v145
	v_bfe_u32 v164, v145, 2, 2
	v_cmp_eq_u32_e64 s[12:13], v163, v164
	s_mov_b32 s50, 0x1c100
	v_mov_b32_e32 v230, 0
	v_mov_b32_e32 v231, 0
	v_mov_b32_e32 v232, 0
	v_mov_b32_e32 v233, 0
	v_mov_b32_e32 v148, 0
	v_mov_b32_e32 v150, 0
	v_mov_b32_e32 v234, 0
	v_mov_b32_e32 v235, 0
	v_mov_b32_e32 v236, 0
	v_mov_b32_e32 v237, 0
	v_mov_b32_e32 v149, 0
	v_mov_b32_e32 v151, 0
	s_waitcnt lgkmcnt(4)
	v_and_b32_e32 v174, 0xfffff800, v166
	v_lshl_add_u64 v[176:177], v[172:173], 0, v[174:175]
	global_load_dwordx4 v[0:3], v[176:177], off
	global_load_dwordx4 v[4:7], v[176:177], off offset:64
	global_load_dwordx4 v[8:11], v[176:177], off offset:128
	global_load_dwordx4 v[12:15], v[176:177], off offset:192
	s_waitcnt lgkmcnt(2)
	v_and_b32_e32 v174, 0xfffff800, v167
	v_lshl_add_u64 v[176:177], v[172:173], 0, v[174:175]
	global_load_dwordx4 v[16:19], v[176:177], off
	global_load_dwordx4 v[20:23], v[176:177], off offset:64
	global_load_dwordx4 v[24:27], v[176:177], off offset:128
	global_load_dwordx4 v[28:31], v[176:177], off offset:192
	s_waitcnt lgkmcnt(0)
	v_and_b32_e32 v174, 0xfffff800, v168
	v_lshl_add_u64 v[176:177], v[172:173], 0, v[174:175]
	global_load_dwordx4 v[32:35], v[176:177], off
	global_load_dwordx4 v[36:39], v[176:177], off offset:64
	global_load_dwordx4 v[40:43], v[176:177], off offset:128
	global_load_dwordx4 v[44:47], v[176:177], off offset:192
	s_mov_b32 s9, 0
	.p2align 3

.LBB0_1594:
	s_waitcnt lgkmcnt(0)
	v_readfirstlane_b32 s58, v32
	v_readfirstlane_b32 s59, v33
	v_lshlrev_b32_e32 v100, 4, v145
	v_mov_b32_e32 v102, s17
	v_mov_b32_e32 v34, 0
	v_mov_b32_e32 v35, 0
	v_mov_b32_e32 v36, 0
	v_mov_b32_e32 v37, 0
	v_mov_b32_e32 v38, 0
	v_mov_b32_e32 v39, 0
	v_mov_b32_e32 v40, 0
	v_mov_b32_e32 v41, 0
	v_mov_b32_e32 v42, 0
	v_mov_b32_e32 v43, 0
	v_mov_b32_e32 v44, 0
	v_mov_b32_e32 v45, 0
	v_mov_b32_e32 v46, 0
	v_mov_b32_e32 v47, 0
	v_mov_b32_e32 v50, 0
	v_mov_b32_e32 v51, 0
	v_mov_b32_e32 v52, 0
	v_mov_b32_e32 v53, 0
	v_mov_b32_e32 v54, 0
	v_mov_b32_e32 v55, 0
	v_mov_b32_e32 v56, 0
	v_mov_b32_e32 v57, 0
	v_mov_b32_e32 v58, 0
	v_mov_b32_e32 v59, 0
	v_mov_b32_e32 v60, 0
	v_mov_b32_e32 v61, 0
	v_mov_b32_e32 v62, 0
	v_mov_b32_e32 v63, 0
	v_mov_b32_e32 v64, 0
	v_mov_b32_e32 v65, 0
	v_mov_b32_e32 v66, 0
	v_mov_b32_e32 v67, 0
	v_mov_b32_e32 v68, 0
	v_mov_b32_e32 v69, 0
	v_mov_b32_e32 v70, 0
	v_mov_b32_e32 v71, 0
	v_mov_b32_e32 v72, 0
	v_mov_b32_e32 v73, 0
	v_mov_b32_e32 v74, 0
	v_mov_b32_e32 v75, 0
	v_mov_b32_e32 v76, 0
	v_mov_b32_e32 v77, 0
	v_mov_b32_e32 v78, 0
	v_mov_b32_e32 v79, 0
	v_mov_b32_e32 v80, 0
	v_mov_b32_e32 v81, 0
	v_mov_b32_e32 v82, 0
	v_mov_b32_e32 v83, 0
	v_mov_b32_e32 v84, 0
	v_mov_b32_e32 v85, 0
	v_mov_b32_e32 v86, 0
	v_mov_b32_e32 v87, 0
	v_mov_b32_e32 v88, 0
	v_mov_b32_e32 v89, 0
	v_mov_b32_e32 v90, 0
	v_mov_b32_e32 v91, 0
	v_mov_b32_e32 v92, 0
	v_mov_b32_e32 v93, 0
	v_mov_b32_e32 v94, 0
	v_mov_b32_e32 v95, 0
	v_mov_b32_e32 v96, 0
	v_mov_b32_e32 v97, 0
	v_mov_b32_e32 v98, 0
	v_mov_b32_e32 v99, 0
	ds_read_b128 v[212:215], v102
	ds_read_b128 v[216:219], v102 offset:16
	s_waitcnt lgkmcnt(0)
	v_readfirstlane_b32 s60, v212
	v_readfirstlane_b32 s61, v213
	v_readfirstlane_b32 s62, v214
	v_readfirstlane_b32 s63, v215
	s_lshl_b32 s60, s60, 11
	v_add_u32_e32 v101, s60, v100
	global_load_dwordx4 v[148:151], v101, s[58:59]
	global_load_dwordx4 v[152:155], v101, s[58:59] offset:1024
	s_lshl_b32 s61, s61, 11
	v_add_u32_e32 v101, s61, v100
	global_load_dwordx4 v[156:159], v101, s[58:59]
	global_load_dwordx4 v[160:163], v101, s[58:59] offset:1024
	s_lshl_b32 s62, s62, 11
	v_add_u32_e32 v101, s62, v100
	global_load_dwordx4 v[164:167], v101, s[58:59]
	global_load_dwordx4 v[168:171], v101, s[58:59] offset:1024
	s_lshl_b32 s63, s63, 11
	v_add_u32_e32 v101, s63, v100
	global_load_dwordx4 v[172:175], v101, s[58:59]
	global_load_dwordx4 v[176:179], v101, s[58:59] offset:1024
	v_readfirstlane_b32 s60, v216
	v_readfirstlane_b32 s61, v217
	v_readfirstlane_b32 s62, v218
	v_readfirstlane_b32 s63, v219
	s_lshl_b32 s60, s60, 11
	v_add_u32_e32 v101, s60, v100
	global_load_dwordx4 v[180:183], v101, s[58:59]
	global_load_dwordx4 v[184:187], v101, s[58:59] offset:1024
	s_lshl_b32 s61, s61, 11
	v_add_u32_e32 v101, s61, v100
	global_load_dwordx4 v[188:191], v101, s[58:59]
	global_load_dwordx4 v[192:195], v101, s[58:59] offset:1024
	s_lshl_b32 s62, s62, 11
	v_add_u32_e32 v101, s62, v100
	global_load_dwordx4 v[196:199], v101, s[58:59]
	global_load_dwordx4 v[200:203], v101, s[58:59] offset:1024
	s_lshl_b32 s63, s63, 11
	v_add_u32_e32 v101, s63, v100
	global_load_dwordx4 v[204:207], v101, s[58:59]
	global_load_dwordx4 v[208:211], v101, s[58:59] offset:1024
	s_mov_b32 s10, 0
	.p2align 3
